# FoX epilogue: the next output row's four gate loads are issued one row ahead (two register sets, counted vmcnt(4)); placement kept
# baseline (speedup 1.0000x reference)
; __device__ __forceinline__ unsigned cvt_pk_bf16(float lo, float hi) { unsigned r; asm volatile("v_cvt_pk_bf16_f32 %0, %1, %2" : "=v"(r) : "v"(lo), "v"(hi)); return r; }
; __device__ __forceinline__ float bf_lo(unsigned w) { return __uint_as_float(w << 16); }
; __device__ __forceinline__ float bf_hi(unsigned w) { return __uint_as_float(w & 0xffff0000u); }
; __device__ __forceinline__ int crow(int r, int hi) { return (r & 3) + 8 * (r >> 2) + 4 * hi; }
; template <int MODE> ...
;     ...
;     for (int r = 0; r < 16; ++r) { const int orow = qlo + crow(r, hi); const float rl = __builtin_amdgcn_rcpf(li_l[crow(r, hi)]);
; #pragma unroll
;         for (int d0 = 0; d0 < 4; ++d0) { float v = o[d0][r] * rl; float vn = __shfl_xor(v, 1);
;             if ((r32 & 1) == 0) { const int col = d0 * 32 + r32;
;                 if (MODE == 1) { const unsigned g = *(const unsigned*)(gate + (size_t)orow * 1024 + hoff + col); v *= bf_lo(g); vn *= bf_hi(g); }
;                 *(unsigned*)(Ob + (size_t)orow * DM + ocol0 + col) = cvt_pk_bf16(v, vn); } } }
.LBB0_1420:
	s_or_b64 exec, exec, s[0:1]
	ds_read_b32 v5, v160 offset:4
	v_add3_u32 v6, s10, v162, 1
	v_ashrrev_i32_e32 v7, 31, v6
	v_lshlrev_b64 v[8:9], 11, v[6:7]
	v_lshlrev_b64 v[6:7], 12, v[6:7]
	s_waitcnt lgkmcnt(0)
	v_rcp_f32_e32 v5, v5
	v_lshl_add_u64 v[8:9], s[6:7], 0, v[8:9]
	v_lshl_add_u64 v[6:7], s[8:9], 0, v[6:7]
	v_lshl_add_u64 v[242:243], v[8:9], 0, v[2:3]
	global_load_dword v244, v[242:243], off
	global_load_dword v245, v[242:243], off offset:64
	global_load_dword v246, v[242:243], off offset:128
	global_load_dword v247, v[242:243], off offset:192
	v_add_u32_e32 v252, 2, v4
	v_ashrrev_i32_e32 v253, 31, v252
	v_lshlrev_b64 v[252:253], 11, v[252:253]
	v_lshl_add_u64 v[252:253], s[6:7], 0, v[252:253]
	v_lshl_add_u64 v[252:253], v[252:253], 0, v[2:3]
	global_load_dword v248, v[252:253], off
	global_load_dword v249, v[252:253], off offset:64
	global_load_dword v250, v[252:253], off offset:128
	global_load_dword v251, v[252:253], off offset:192
	v_mul_f32_e32 v11, v67, v5
	s_nop 1
	v_mov_b32_dpp v12, v11 quad_perm:[1,0,3,2] row_mask:0xf bank_mask:0xf
	s_and_saveexec_b64 s[0:1], s[2:3]
	s_cbranch_execz .LBB0_1422
	v_lshl_add_u64 v[14:15], v[8:9], 0, v[2:3]
	s_waitcnt vmcnt(4)
	v_mov_b32_e32 v13, v244
	v_lshlrev_b32_e32 v14, 16, v13
	v_and_b32_e32 v13, 0xffff0000, v13
	v_mul_f32_e32 v11, v11, v14
	s_waitcnt lgkmcnt(0)
	v_mul_f32_e32 v12, v12, v13
	v_cvt_pk_bf16_f32 v11, v11, v12
	v_lshl_add_u64 v[12:13], v[6:7], 0, v[2:3]
	global_store_dword v[12:13], v11, off

; __device__ __forceinline__ unsigned cvt_pk_bf16(float lo, float hi) { unsigned r; asm volatile("v_cvt_pk_bf16_f32 %0, %1, %2" : "=v"(r) : "v"(lo), "v"(hi)); return r; }
; __device__ __forceinline__ float bf_lo(unsigned w) { return __uint_as_float(w << 16); }
; __device__ __forceinline__ float bf_hi(unsigned w) { return __uint_as_float(w & 0xffff0000u); }
; __device__ __forceinline__ int crow(int r, int hi) { return (r & 3) + 8 * (r >> 2) + 4 * hi; }
; template <int MODE> ...
;     ...
;     for (int r = 0; r < 16; ++r) { const int orow = qlo + crow(r, hi); const float rl = __builtin_amdgcn_rcpf(li_l[crow(r, hi)]);
; #pragma unroll
;         for (int d0 = 0; d0 < 4; ++d0) { float v = o[d0][r] * rl; float vn = __shfl_xor(v, 1);
;             if ((r32 & 1) == 0) { const int col = d0 * 32 + r32;
;                 if (MODE == 1) { const unsigned g = *(const unsigned*)(gate + (size_t)orow * 1024 + hoff + col); v *= bf_lo(g); vn *= bf_hi(g); }
;                 *(unsigned*)(Ob + (size_t)orow * DM + ocol0 + col) = cvt_pk_bf16(v, vn); } } }
.LBB0_1428:
	s_or_b64 exec, exec, s[0:1]
	ds_read_b32 v5, v160 offset:8
	v_add3_u32 v6, s10, v162, 2
	v_ashrrev_i32_e32 v7, 31, v6
	v_lshlrev_b64 v[8:9], 11, v[6:7]
	v_lshlrev_b64 v[6:7], 12, v[6:7]
	s_waitcnt lgkmcnt(0)
	v_rcp_f32_e32 v5, v5
	v_lshl_add_u64 v[8:9], s[6:7], 0, v[8:9]
	v_lshl_add_u64 v[6:7], s[8:9], 0, v[6:7]
	v_add_u32_e32 v252, 3, v4
	v_ashrrev_i32_e32 v253, 31, v252
	v_lshlrev_b64 v[252:253], 11, v[252:253]
	v_lshl_add_u64 v[252:253], s[6:7], 0, v[252:253]
	v_lshl_add_u64 v[252:253], v[252:253], 0, v[2:3]
	global_load_dword v244, v[252:253], off
	global_load_dword v245, v[252:253], off offset:64
	global_load_dword v246, v[252:253], off offset:128
	global_load_dword v247, v[252:253], off offset:192
	v_mul_f32_e32 v11, v68, v5
	s_nop 1
	v_mov_b32_dpp v12, v11 quad_perm:[1,0,3,2] row_mask:0xf bank_mask:0xf
	s_and_saveexec_b64 s[0:1], s[2:3]
	s_cbranch_execz .LBB0_1430
	v_lshl_add_u64 v[14:15], v[8:9], 0, v[2:3]
	s_waitcnt vmcnt(4)
	v_mov_b32_e32 v13, v248
	v_lshlrev_b32_e32 v14, 16, v13
	v_and_b32_e32 v13, 0xffff0000, v13
	v_mul_f32_e32 v11, v11, v14
	s_waitcnt lgkmcnt(0)
	v_mul_f32_e32 v12, v12, v13
	v_cvt_pk_bf16_f32 v11, v11, v12
	v_lshl_add_u64 v[12:13], v[6:7], 0, v[2:3]
	global_store_dword v[12:13], v11, off
.LBB0_1430:
	s_or_b64 exec, exec, s[0:1]
	v_mul_f32_e32 v11, v52, v5
	s_waitcnt lgkmcnt(0)
	s_nop 1
	v_mov_b32_dpp v12, v11 quad_perm:[1,0,3,2] row_mask:0xf bank_mask:0xf
	s_and_saveexec_b64 s[0:1], s[2:3]
	s_cbranch_execz .LBB0_1432
	v_lshl_add_u64 v[14:15], v[8:9], 0, v[2:3]
	v_mov_b32_e32 v13, v249
	v_lshlrev_b32_e32 v14, 16, v13
	v_and_b32_e32 v13, 0xffff0000, v13
	v_mul_f32_e32 v11, v11, v14
	s_waitcnt lgkmcnt(0)
	v_mul_f32_e32 v12, v12, v13
	v_cvt_pk_bf16_f32 v11, v11, v12
	v_lshl_add_u64 v[12:13], v[6:7], 0, v[2:3]
	global_store_dword v[12:13], v11, off offset:64
.LBB0_1432:
	s_or_b64 exec, exec, s[0:1]
	v_mul_f32_e32 v11, v36, v5
	s_waitcnt lgkmcnt(0)
	s_nop 1
	v_mov_b32_dpp v12, v11 quad_perm:[1,0,3,2] row_mask:0xf bank_mask:0xf
	s_and_saveexec_b64 s[0:1], s[2:3]
	s_cbranch_execz .LBB0_1434
	v_lshl_add_u64 v[14:15], v[8:9], 0, v[2:3]
	v_mov_b32_e32 v13, v250
	v_lshlrev_b32_e32 v14, 16, v13
	v_and_b32_e32 v13, 0xffff0000, v13
	v_mul_f32_e32 v11, v11, v14
	s_waitcnt lgkmcnt(0)
	v_mul_f32_e32 v12, v12, v13
	v_cvt_pk_bf16_f32 v11, v11, v12
	v_lshl_add_u64 v[12:13], v[6:7], 0, v[2:3]
	global_store_dword v[12:13], v11, off offset:128
.LBB0_1434:
	s_or_b64 exec, exec, s[0:1]
	v_mul_f32_e32 v5, v20, v5
	s_nop 1
	v_mov_b32_dpp v11, v5 quad_perm:[1,0,3,2] row_mask:0xf bank_mask:0xf
	s_and_saveexec_b64 s[0:1], s[2:3]
	s_cbranch_execz .LBB0_1436
	v_lshl_add_u64 v[8:9], v[8:9], 0, v[2:3]
	v_lshl_add_u64 v[6:7], v[6:7], 0, v[2:3]
	v_mov_b32_e32 v8, v251
	v_lshlrev_b32_e32 v9, 16, v8
	v_and_b32_e32 v8, 0xffff0000, v8
	v_mul_f32_e32 v5, v5, v9
	s_waitcnt lgkmcnt(0)
	v_mul_f32_e32 v8, v11, v8
	v_cvt_pk_bf16_f32 v5, v5, v8
	global_store_dword v[6:7], v5, off offset:192
.LBB0_1436:
	s_or_b64 exec, exec, s[0:1]
	ds_read_b32 v5, v160 offset:12
	v_add3_u32 v6, s10, v162, 3
	v_ashrrev_i32_e32 v7, 31, v6
	v_lshlrev_b64 v[8:9], 11, v[6:7]
	v_lshlrev_b64 v[6:7], 12, v[6:7]
	s_waitcnt lgkmcnt(0)
	v_rcp_f32_e32 v5, v5
	v_lshl_add_u64 v[8:9], s[6:7], 0, v[8:9]
	v_lshl_add_u64 v[6:7], s[8:9], 0, v[6:7]
	v_add_u32_e32 v252, 8, v4
	v_ashrrev_i32_e32 v253, 31, v252
	v_lshlrev_b64 v[252:253], 11, v[252:253]
	v_lshl_add_u64 v[252:253], s[6:7], 0, v[252:253]
	v_lshl_add_u64 v[252:253], v[252:253], 0, v[2:3]
	global_load_dword v248, v[252:253], off
	global_load_dword v249, v[252:253], off offset:64
	global_load_dword v250, v[252:253], off offset:128
	global_load_dword v251, v[252:253], off offset:192
	v_mul_f32_e32 v11, v69, v5
	s_nop 1
	v_mov_b32_dpp v12, v11 quad_perm:[1,0,3,2] row_mask:0xf bank_mask:0xf
	s_and_saveexec_b64 s[0:1], s[2:3]
	s_cbranch_execz .LBB0_1438
	v_lshl_add_u64 v[14:15], v[8:9], 0, v[2:3]
	s_waitcnt vmcnt(4)
	v_mov_b32_e32 v13, v244
	v_lshlrev_b32_e32 v14, 16, v13
	v_and_b32_e32 v13, 0xffff0000, v13
	v_mul_f32_e32 v11, v11, v14
	s_waitcnt lgkmcnt(0)
	v_mul_f32_e32 v12, v12, v13
	v_cvt_pk_bf16_f32 v11, v11, v12
	v_lshl_add_u64 v[12:13], v[6:7], 0, v[2:3]
	global_store_dword v[12:13], v11, off

; __device__ __forceinline__ unsigned cvt_pk_bf16(float lo, float hi) { unsigned r; asm volatile("v_cvt_pk_bf16_f32 %0, %1, %2" : "=v"(r) : "v"(lo), "v"(hi)); return r; }
; __device__ __forceinline__ float bf_lo(unsigned w) { return __uint_as_float(w << 16); }
; __device__ __forceinline__ float bf_hi(unsigned w) { return __uint_as_float(w & 0xffff0000u); }
; __device__ __forceinline__ int crow(int r, int hi) { return (r & 3) + 8 * (r >> 2) + 4 * hi; }
; template <int MODE> ...
;     ...
;     for (int r = 0; r < 16; ++r) { const int orow = qlo + crow(r, hi); const float rl = __builtin_amdgcn_rcpf(li_l[crow(r, hi)]);
; #pragma unroll
;         for (int d0 = 0; d0 < 4; ++d0) { float v = o[d0][r] * rl; float vn = __shfl_xor(v, 1);
;             if ((r32 & 1) == 0) { const int col = d0 * 32 + r32;
;                 if (MODE == 1) { const unsigned g = *(const unsigned*)(gate + (size_t)orow * 1024 + hoff + col); v *= bf_lo(g); vn *= bf_hi(g); }
;                 *(unsigned*)(Ob + (size_t)orow * DM + ocol0 + col) = cvt_pk_bf16(v, vn); } } }
.LBB0_1444:
	s_or_b64 exec, exec, s[0:1]
	ds_read_b32 v5, v160 offset:32
	v_add_u32_e32 v6, 8, v4
	v_ashrrev_i32_e32 v7, 31, v6
	v_lshlrev_b64 v[8:9], 11, v[6:7]
	v_lshlrev_b64 v[6:7], 12, v[6:7]
	s_waitcnt lgkmcnt(0)
	v_rcp_f32_e32 v5, v5
	v_lshl_add_u64 v[8:9], s[6:7], 0, v[8:9]
	v_lshl_add_u64 v[6:7], s[8:9], 0, v[6:7]
	v_add_u32_e32 v252, 9, v4
	v_ashrrev_i32_e32 v253, 31, v252
	v_lshlrev_b64 v[252:253], 11, v[252:253]
	v_lshl_add_u64 v[252:253], s[6:7], 0, v[252:253]
	v_lshl_add_u64 v[252:253], v[252:253], 0, v[2:3]
	global_load_dword v244, v[252:253], off
	global_load_dword v245, v[252:253], off offset:64
	global_load_dword v246, v[252:253], off offset:128
	global_load_dword v247, v[252:253], off offset:192
	v_mul_f32_e32 v11, v70, v5
	s_nop 1
	v_mov_b32_dpp v12, v11 quad_perm:[1,0,3,2] row_mask:0xf bank_mask:0xf
	s_and_saveexec_b64 s[0:1], s[2:3]
	s_cbranch_execz .LBB0_1446
	v_lshl_add_u64 v[14:15], v[8:9], 0, v[2:3]
	s_waitcnt vmcnt(4)
	v_mov_b32_e32 v13, v248
	v_lshlrev_b32_e32 v14, 16, v13
	v_and_b32_e32 v13, 0xffff0000, v13
	v_mul_f32_e32 v11, v11, v14
	s_waitcnt lgkmcnt(0)
	v_mul_f32_e32 v12, v12, v13
	v_cvt_pk_bf16_f32 v11, v11, v12
	v_lshl_add_u64 v[12:13], v[6:7], 0, v[2:3]
	global_store_dword v[12:13], v11, off
.LBB0_1446:
	s_or_b64 exec, exec, s[0:1]
	v_mul_f32_e32 v11, v54, v5
	s_waitcnt lgkmcnt(0)
	s_nop 1
	v_mov_b32_dpp v12, v11 quad_perm:[1,0,3,2] row_mask:0xf bank_mask:0xf
	s_and_saveexec_b64 s[0:1], s[2:3]
	s_cbranch_execz .LBB0_1448
	v_lshl_add_u64 v[14:15], v[8:9], 0, v[2:3]
	v_mov_b32_e32 v13, v249
	v_lshlrev_b32_e32 v14, 16, v13
	v_and_b32_e32 v13, 0xffff0000, v13
	v_mul_f32_e32 v11, v11, v14
	s_waitcnt lgkmcnt(0)
	v_mul_f32_e32 v12, v12, v13
	v_cvt_pk_bf16_f32 v11, v11, v12
	v_lshl_add_u64 v[12:13], v[6:7], 0, v[2:3]
	global_store_dword v[12:13], v11, off offset:64
.LBB0_1448:
	s_or_b64 exec, exec, s[0:1]
	v_mul_f32_e32 v11, v38, v5
	s_waitcnt lgkmcnt(0)
	s_nop 1
	v_mov_b32_dpp v12, v11 quad_perm:[1,0,3,2] row_mask:0xf bank_mask:0xf
	s_and_saveexec_b64 s[0:1], s[2:3]
	s_cbranch_execz .LBB0_1450
	v_lshl_add_u64 v[14:15], v[8:9], 0, v[2:3]
	v_mov_b32_e32 v13, v250
	v_lshlrev_b32_e32 v14, 16, v13
	v_and_b32_e32 v13, 0xffff0000, v13
	v_mul_f32_e32 v11, v11, v14
	s_waitcnt lgkmcnt(0)
	v_mul_f32_e32 v12, v12, v13
	v_cvt_pk_bf16_f32 v11, v11, v12
	v_lshl_add_u64 v[12:13], v[6:7], 0, v[2:3]
	global_store_dword v[12:13], v11, off offset:128
.LBB0_1450:
	s_or_b64 exec, exec, s[0:1]
	v_mul_f32_e32 v5, v22, v5
	s_nop 1
	v_mov_b32_dpp v11, v5 quad_perm:[1,0,3,2] row_mask:0xf bank_mask:0xf
	s_and_saveexec_b64 s[0:1], s[2:3]
	s_cbranch_execz .LBB0_1452
	v_lshl_add_u64 v[8:9], v[8:9], 0, v[2:3]
	v_lshl_add_u64 v[6:7], v[6:7], 0, v[2:3]
	v_mov_b32_e32 v8, v251
	v_lshlrev_b32_e32 v9, 16, v8
	v_and_b32_e32 v8, 0xffff0000, v8
	v_mul_f32_e32 v5, v5, v9
	s_waitcnt lgkmcnt(0)
	v_mul_f32_e32 v8, v11, v8
	v_cvt_pk_bf16_f32 v5, v5, v8
	global_store_dword v[6:7], v5, off offset:192
.LBB0_1452:
	s_or_b64 exec, exec, s[0:1]
	ds_read_b32 v5, v160 offset:36
	v_add_u32_e32 v6, 9, v4
	v_ashrrev_i32_e32 v7, 31, v6
	v_lshlrev_b64 v[8:9], 11, v[6:7]
	v_lshlrev_b64 v[6:7], 12, v[6:7]
	s_waitcnt lgkmcnt(0)
	v_rcp_f32_e32 v5, v5
	v_lshl_add_u64 v[8:9], s[6:7], 0, v[8:9]
	v_lshl_add_u64 v[6:7], s[8:9], 0, v[6:7]
	v_add_u32_e32 v252, 10, v4
	v_ashrrev_i32_e32 v253, 31, v252
	v_lshlrev_b64 v[252:253], 11, v[252:253]
	v_lshl_add_u64 v[252:253], s[6:7], 0, v[252:253]
	v_lshl_add_u64 v[252:253], v[252:253], 0, v[2:3]
	global_load_dword v248, v[252:253], off
	global_load_dword v249, v[252:253], off offset:64
	global_load_dword v250, v[252:253], off offset:128
	global_load_dword v251, v[252:253], off offset:192
	v_mul_f32_e32 v11, v71, v5
	s_nop 1
	v_mov_b32_dpp v12, v11 quad_perm:[1,0,3,2] row_mask:0xf bank_mask:0xf
	s_and_saveexec_b64 s[0:1], s[2:3]
	s_cbranch_execz .LBB0_1454
	v_lshl_add_u64 v[14:15], v[8:9], 0, v[2:3]
	s_waitcnt vmcnt(4)
	v_mov_b32_e32 v13, v244
	v_lshlrev_b32_e32 v14, 16, v13
	v_and_b32_e32 v13, 0xffff0000, v13
	v_mul_f32_e32 v11, v11, v14
	s_waitcnt lgkmcnt(0)
	v_mul_f32_e32 v12, v12, v13
	v_cvt_pk_bf16_f32 v11, v11, v12
	v_lshl_add_u64 v[12:13], v[6:7], 0, v[2:3]
	global_store_dword v[12:13], v11, off

; __device__ __forceinline__ unsigned cvt_pk_bf16(float lo, float hi) { unsigned r; asm volatile("v_cvt_pk_bf16_f32 %0, %1, %2" : "=v"(r) : "v"(lo), "v"(hi)); return r; }
; __device__ __forceinline__ float bf_lo(unsigned w) { return __uint_as_float(w << 16); }
; __device__ __forceinline__ float bf_hi(unsigned w) { return __uint_as_float(w & 0xffff0000u); }
; __device__ __forceinline__ int crow(int r, int hi) { return (r & 3) + 8 * (r >> 2) + 4 * hi; }
; template <int MODE> ...
;     ...
;     for (int r = 0; r < 16; ++r) { const int orow = qlo + crow(r, hi); const float rl = __builtin_amdgcn_rcpf(li_l[crow(r, hi)]);
; #pragma unroll
;         for (int d0 = 0; d0 < 4; ++d0) { float v = o[d0][r] * rl; float vn = __shfl_xor(v, 1);
;             if ((r32 & 1) == 0) { const int col = d0 * 32 + r32;
;                 if (MODE == 1) { const unsigned g = *(const unsigned*)(gate + (size_t)orow * 1024 + hoff + col); v *= bf_lo(g); vn *= bf_hi(g); }
;                 *(unsigned*)(Ob + (size_t)orow * DM + ocol0 + col) = cvt_pk_bf16(v, vn); } } }
.LBB0_1460:
	s_or_b64 exec, exec, s[0:1]
	ds_read_b32 v5, v160 offset:40
	v_add_u32_e32 v6, 10, v4
	v_ashrrev_i32_e32 v7, 31, v6
	v_lshlrev_b64 v[8:9], 11, v[6:7]
	v_lshlrev_b64 v[6:7], 12, v[6:7]
	s_waitcnt lgkmcnt(0)
	v_rcp_f32_e32 v5, v5
	v_lshl_add_u64 v[8:9], s[6:7], 0, v[8:9]
	v_lshl_add_u64 v[6:7], s[8:9], 0, v[6:7]
	v_add_u32_e32 v252, 11, v4
	v_ashrrev_i32_e32 v253, 31, v252
	v_lshlrev_b64 v[252:253], 11, v[252:253]
	v_lshl_add_u64 v[252:253], s[6:7], 0, v[252:253]
	v_lshl_add_u64 v[252:253], v[252:253], 0, v[2:3]
	global_load_dword v244, v[252:253], off
	global_load_dword v245, v[252:253], off offset:64
	global_load_dword v246, v[252:253], off offset:128
	global_load_dword v247, v[252:253], off offset:192
	v_mul_f32_e32 v11, v72, v5
	s_nop 1
	v_mov_b32_dpp v12, v11 quad_perm:[1,0,3,2] row_mask:0xf bank_mask:0xf
	s_and_saveexec_b64 s[0:1], s[2:3]
	s_cbranch_execz .LBB0_1462
	v_lshl_add_u64 v[14:15], v[8:9], 0, v[2:3]
	s_waitcnt vmcnt(4)
	v_mov_b32_e32 v13, v248
	v_lshlrev_b32_e32 v14, 16, v13
	v_and_b32_e32 v13, 0xffff0000, v13
	v_mul_f32_e32 v11, v11, v14
	s_waitcnt lgkmcnt(0)
	v_mul_f32_e32 v12, v12, v13
	v_cvt_pk_bf16_f32 v11, v11, v12
	v_lshl_add_u64 v[12:13], v[6:7], 0, v[2:3]
	global_store_dword v[12:13], v11, off
.LBB0_1462:
	s_or_b64 exec, exec, s[0:1]
	v_mul_f32_e32 v11, v56, v5
	s_waitcnt lgkmcnt(0)
	s_nop 1
	v_mov_b32_dpp v12, v11 quad_perm:[1,0,3,2] row_mask:0xf bank_mask:0xf
	s_and_saveexec_b64 s[0:1], s[2:3]
	s_cbranch_execz .LBB0_1464
	v_lshl_add_u64 v[14:15], v[8:9], 0, v[2:3]
	v_mov_b32_e32 v13, v249
	v_lshlrev_b32_e32 v14, 16, v13
	v_and_b32_e32 v13, 0xffff0000, v13
	v_mul_f32_e32 v11, v11, v14
	s_waitcnt lgkmcnt(0)
	v_mul_f32_e32 v12, v12, v13
	v_cvt_pk_bf16_f32 v11, v11, v12
	v_lshl_add_u64 v[12:13], v[6:7], 0, v[2:3]
	global_store_dword v[12:13], v11, off offset:64
.LBB0_1464:
	s_or_b64 exec, exec, s[0:1]
	v_mul_f32_e32 v11, v40, v5
	s_waitcnt lgkmcnt(0)
	s_nop 1
	v_mov_b32_dpp v12, v11 quad_perm:[1,0,3,2] row_mask:0xf bank_mask:0xf
	s_and_saveexec_b64 s[0:1], s[2:3]
	s_cbranch_execz .LBB0_1466
	v_lshl_add_u64 v[14:15], v[8:9], 0, v[2:3]
	v_mov_b32_e32 v13, v250
	v_lshlrev_b32_e32 v14, 16, v13
	v_and_b32_e32 v13, 0xffff0000, v13
	v_mul_f32_e32 v11, v11, v14
	s_waitcnt lgkmcnt(0)
	v_mul_f32_e32 v12, v12, v13
	v_cvt_pk_bf16_f32 v11, v11, v12
	v_lshl_add_u64 v[12:13], v[6:7], 0, v[2:3]
	global_store_dword v[12:13], v11, off offset:128
.LBB0_1466:
	s_or_b64 exec, exec, s[0:1]
	v_mul_f32_e32 v5, v24, v5
	s_nop 1
	v_mov_b32_dpp v11, v5 quad_perm:[1,0,3,2] row_mask:0xf bank_mask:0xf
	s_and_saveexec_b64 s[0:1], s[2:3]
	s_cbranch_execz .LBB0_1468
	v_lshl_add_u64 v[8:9], v[8:9], 0, v[2:3]
	v_lshl_add_u64 v[6:7], v[6:7], 0, v[2:3]
	v_mov_b32_e32 v8, v251
	v_lshlrev_b32_e32 v9, 16, v8
	v_and_b32_e32 v8, 0xffff0000, v8
	v_mul_f32_e32 v5, v5, v9
	s_waitcnt lgkmcnt(0)
	v_mul_f32_e32 v8, v11, v8
	v_cvt_pk_bf16_f32 v5, v5, v8
	global_store_dword v[6:7], v5, off offset:192
.LBB0_1468:
	s_or_b64 exec, exec, s[0:1]
	ds_read_b32 v5, v160 offset:44
	v_add_u32_e32 v6, 11, v4
	v_ashrrev_i32_e32 v7, 31, v6
	v_lshlrev_b64 v[8:9], 11, v[6:7]
	v_lshlrev_b64 v[6:7], 12, v[6:7]
	s_waitcnt lgkmcnt(0)
	v_rcp_f32_e32 v5, v5
	v_lshl_add_u64 v[8:9], s[6:7], 0, v[8:9]
	v_lshl_add_u64 v[6:7], s[8:9], 0, v[6:7]
	v_add_u32_e32 v252, 16, v4
	v_ashrrev_i32_e32 v253, 31, v252
	v_lshlrev_b64 v[252:253], 11, v[252:253]
	v_lshl_add_u64 v[252:253], s[6:7], 0, v[252:253]
	v_lshl_add_u64 v[252:253], v[252:253], 0, v[2:3]
	global_load_dword v248, v[252:253], off
	global_load_dword v249, v[252:253], off offset:64
	global_load_dword v250, v[252:253], off offset:128
	global_load_dword v251, v[252:253], off offset:192
	v_mul_f32_e32 v11, v73, v5
	s_nop 1
	v_mov_b32_dpp v12, v11 quad_perm:[1,0,3,2] row_mask:0xf bank_mask:0xf
	s_and_saveexec_b64 s[0:1], s[2:3]
	s_cbranch_execz .LBB0_1470
	v_lshl_add_u64 v[14:15], v[8:9], 0, v[2:3]
	s_waitcnt vmcnt(4)
	v_mov_b32_e32 v13, v244
	v_lshlrev_b32_e32 v14, 16, v13
	v_and_b32_e32 v13, 0xffff0000, v13
	v_mul_f32_e32 v11, v11, v14
	s_waitcnt lgkmcnt(0)
	v_mul_f32_e32 v12, v12, v13
	v_cvt_pk_bf16_f32 v11, v11, v12
	v_lshl_add_u64 v[12:13], v[6:7], 0, v[2:3]
	global_store_dword v[12:13], v11, off

; __device__ __forceinline__ unsigned cvt_pk_bf16(float lo, float hi) { unsigned r; asm volatile("v_cvt_pk_bf16_f32 %0, %1, %2" : "=v"(r) : "v"(lo), "v"(hi)); return r; }
; __device__ __forceinline__ float bf_lo(unsigned w) { return __uint_as_float(w << 16); }
; __device__ __forceinline__ float bf_hi(unsigned w) { return __uint_as_float(w & 0xffff0000u); }
; __device__ __forceinline__ int crow(int r, int hi) { return (r & 3) + 8 * (r >> 2) + 4 * hi; }
; template <int MODE> ...
;     ...
;     for (int r = 0; r < 16; ++r) { const int orow = qlo + crow(r, hi); const float rl = __builtin_amdgcn_rcpf(li_l[crow(r, hi)]);
; #pragma unroll
;         for (int d0 = 0; d0 < 4; ++d0) { float v = o[d0][r] * rl; float vn = __shfl_xor(v, 1);
;             if ((r32 & 1) == 0) { const int col = d0 * 32 + r32;
;                 if (MODE == 1) { const unsigned g = *(const unsigned*)(gate + (size_t)orow * 1024 + hoff + col); v *= bf_lo(g); vn *= bf_hi(g); }
;                 *(unsigned*)(Ob + (size_t)orow * DM + ocol0 + col) = cvt_pk_bf16(v, vn); } } }
.LBB0_1476:
	s_or_b64 exec, exec, s[0:1]
	ds_read_b32 v5, v160 offset:64
	v_add_u32_e32 v6, 16, v4
	v_ashrrev_i32_e32 v7, 31, v6
	v_lshlrev_b64 v[8:9], 11, v[6:7]
	v_lshlrev_b64 v[6:7], 12, v[6:7]
	s_waitcnt lgkmcnt(0)
	v_rcp_f32_e32 v5, v5
	v_lshl_add_u64 v[8:9], s[6:7], 0, v[8:9]
	v_lshl_add_u64 v[6:7], s[8:9], 0, v[6:7]
	v_add_u32_e32 v252, 17, v4
	v_ashrrev_i32_e32 v253, 31, v252
	v_lshlrev_b64 v[252:253], 11, v[252:253]
	v_lshl_add_u64 v[252:253], s[6:7], 0, v[252:253]
	v_lshl_add_u64 v[252:253], v[252:253], 0, v[2:3]
	global_load_dword v244, v[252:253], off
	global_load_dword v245, v[252:253], off offset:64
	global_load_dword v246, v[252:253], off offset:128
	global_load_dword v247, v[252:253], off offset:192
	v_mul_f32_e32 v11, v74, v5
	s_nop 1
	v_mov_b32_dpp v12, v11 quad_perm:[1,0,3,2] row_mask:0xf bank_mask:0xf
	s_and_saveexec_b64 s[0:1], s[2:3]
	s_cbranch_execz .LBB0_1478
	v_lshl_add_u64 v[14:15], v[8:9], 0, v[2:3]
	s_waitcnt vmcnt(4)
	v_mov_b32_e32 v13, v248
	v_lshlrev_b32_e32 v14, 16, v13
	v_and_b32_e32 v13, 0xffff0000, v13
	v_mul_f32_e32 v11, v11, v14
	s_waitcnt lgkmcnt(0)
	v_mul_f32_e32 v12, v12, v13
	v_cvt_pk_bf16_f32 v11, v11, v12
	v_lshl_add_u64 v[12:13], v[6:7], 0, v[2:3]
	global_store_dword v[12:13], v11, off
.LBB0_1478:
	s_or_b64 exec, exec, s[0:1]
	v_mul_f32_e32 v11, v58, v5
	s_waitcnt lgkmcnt(0)
	s_nop 1
	v_mov_b32_dpp v12, v11 quad_perm:[1,0,3,2] row_mask:0xf bank_mask:0xf
	s_and_saveexec_b64 s[0:1], s[2:3]
	s_cbranch_execz .LBB0_1480
	v_lshl_add_u64 v[14:15], v[8:9], 0, v[2:3]
	v_mov_b32_e32 v13, v249
	v_lshlrev_b32_e32 v14, 16, v13
	v_and_b32_e32 v13, 0xffff0000, v13
	v_mul_f32_e32 v11, v11, v14
	s_waitcnt lgkmcnt(0)
	v_mul_f32_e32 v12, v12, v13
	v_cvt_pk_bf16_f32 v11, v11, v12
	v_lshl_add_u64 v[12:13], v[6:7], 0, v[2:3]
	global_store_dword v[12:13], v11, off offset:64
.LBB0_1480:
	s_or_b64 exec, exec, s[0:1]
	v_mul_f32_e32 v11, v42, v5
	s_waitcnt lgkmcnt(0)
	s_nop 1
	v_mov_b32_dpp v12, v11 quad_perm:[1,0,3,2] row_mask:0xf bank_mask:0xf
	s_and_saveexec_b64 s[0:1], s[2:3]
	s_cbranch_execz .LBB0_1482
	v_lshl_add_u64 v[14:15], v[8:9], 0, v[2:3]
	v_mov_b32_e32 v13, v250
	v_lshlrev_b32_e32 v14, 16, v13
	v_and_b32_e32 v13, 0xffff0000, v13
	v_mul_f32_e32 v11, v11, v14
	s_waitcnt lgkmcnt(0)
	v_mul_f32_e32 v12, v12, v13
	v_cvt_pk_bf16_f32 v11, v11, v12
	v_lshl_add_u64 v[12:13], v[6:7], 0, v[2:3]
	global_store_dword v[12:13], v11, off offset:128
.LBB0_1482:
	s_or_b64 exec, exec, s[0:1]
	v_mul_f32_e32 v5, v26, v5
	s_nop 1
	v_mov_b32_dpp v11, v5 quad_perm:[1,0,3,2] row_mask:0xf bank_mask:0xf
	s_and_saveexec_b64 s[0:1], s[2:3]
	s_cbranch_execz .LBB0_1484
	v_lshl_add_u64 v[8:9], v[8:9], 0, v[2:3]
	v_lshl_add_u64 v[6:7], v[6:7], 0, v[2:3]
	v_mov_b32_e32 v8, v251
	v_lshlrev_b32_e32 v9, 16, v8
	v_and_b32_e32 v8, 0xffff0000, v8
	v_mul_f32_e32 v5, v5, v9
	s_waitcnt lgkmcnt(0)
	v_mul_f32_e32 v8, v11, v8
	v_cvt_pk_bf16_f32 v5, v5, v8
	global_store_dword v[6:7], v5, off offset:192
.LBB0_1484:
	s_or_b64 exec, exec, s[0:1]
	ds_read_b32 v5, v160 offset:68
	v_add_u32_e32 v6, 17, v4
	v_ashrrev_i32_e32 v7, 31, v6
	v_lshlrev_b64 v[8:9], 11, v[6:7]
	v_lshlrev_b64 v[6:7], 12, v[6:7]
	s_waitcnt lgkmcnt(0)
	v_rcp_f32_e32 v5, v5
	v_lshl_add_u64 v[8:9], s[6:7], 0, v[8:9]
	v_lshl_add_u64 v[6:7], s[8:9], 0, v[6:7]
	v_add_u32_e32 v252, 18, v4
	v_ashrrev_i32_e32 v253, 31, v252
	v_lshlrev_b64 v[252:253], 11, v[252:253]
	v_lshl_add_u64 v[252:253], s[6:7], 0, v[252:253]
	v_lshl_add_u64 v[252:253], v[252:253], 0, v[2:3]
	global_load_dword v248, v[252:253], off
	global_load_dword v249, v[252:253], off offset:64
	global_load_dword v250, v[252:253], off offset:128
	global_load_dword v251, v[252:253], off offset:192
	v_mul_f32_e32 v11, v75, v5
	s_nop 1
	v_mov_b32_dpp v12, v11 quad_perm:[1,0,3,2] row_mask:0xf bank_mask:0xf
	s_and_saveexec_b64 s[0:1], s[2:3]
	s_cbranch_execz .LBB0_1486
	v_lshl_add_u64 v[14:15], v[8:9], 0, v[2:3]
	s_waitcnt vmcnt(4)
	v_mov_b32_e32 v13, v244
	v_lshlrev_b32_e32 v14, 16, v13
	v_and_b32_e32 v13, 0xffff0000, v13
	v_mul_f32_e32 v11, v11, v14
	s_waitcnt lgkmcnt(0)
	v_mul_f32_e32 v12, v12, v13
	v_cvt_pk_bf16_f32 v11, v11, v12
	v_lshl_add_u64 v[12:13], v[6:7], 0, v[2:3]
	global_store_dword v[12:13], v11, off

; __device__ __forceinline__ unsigned cvt_pk_bf16(float lo, float hi) { unsigned r; asm volatile("v_cvt_pk_bf16_f32 %0, %1, %2" : "=v"(r) : "v"(lo), "v"(hi)); return r; }
; __device__ __forceinline__ float bf_lo(unsigned w) { return __uint_as_float(w << 16); }
; __device__ __forceinline__ float bf_hi(unsigned w) { return __uint_as_float(w & 0xffff0000u); }
; __device__ __forceinline__ int crow(int r, int hi) { return (r & 3) + 8 * (r >> 2) + 4 * hi; }
; template <int MODE> ...
;     ...
;     for (int r = 0; r < 16; ++r) { const int orow = qlo + crow(r, hi); const float rl = __builtin_amdgcn_rcpf(li_l[crow(r, hi)]);
; #pragma unroll
;         for (int d0 = 0; d0 < 4; ++d0) { float v = o[d0][r] * rl; float vn = __shfl_xor(v, 1);
;             if ((r32 & 1) == 0) { const int col = d0 * 32 + r32;
;                 if (MODE == 1) { const unsigned g = *(const unsigned*)(gate + (size_t)orow * 1024 + hoff + col); v *= bf_lo(g); vn *= bf_hi(g); }
;                 *(unsigned*)(Ob + (size_t)orow * DM + ocol0 + col) = cvt_pk_bf16(v, vn); } } }
.LBB0_1492:
	s_or_b64 exec, exec, s[0:1]
	ds_read_b32 v5, v160 offset:72
	v_add_u32_e32 v6, 18, v4
	v_ashrrev_i32_e32 v7, 31, v6
	v_lshlrev_b64 v[8:9], 11, v[6:7]
	v_lshlrev_b64 v[6:7], 12, v[6:7]
	s_waitcnt lgkmcnt(0)
	v_rcp_f32_e32 v5, v5
	v_lshl_add_u64 v[8:9], s[6:7], 0, v[8:9]
	v_lshl_add_u64 v[6:7], s[8:9], 0, v[6:7]
	v_add_u32_e32 v252, 19, v4
	v_ashrrev_i32_e32 v253, 31, v252
	v_lshlrev_b64 v[252:253], 11, v[252:253]
	v_lshl_add_u64 v[252:253], s[6:7], 0, v[252:253]
	v_lshl_add_u64 v[252:253], v[252:253], 0, v[2:3]
	global_load_dword v244, v[252:253], off
	global_load_dword v245, v[252:253], off offset:64
	global_load_dword v246, v[252:253], off offset:128
	global_load_dword v247, v[252:253], off offset:192
	v_mul_f32_e32 v11, v76, v5
	s_nop 1
	v_mov_b32_dpp v12, v11 quad_perm:[1,0,3,2] row_mask:0xf bank_mask:0xf
	s_and_saveexec_b64 s[0:1], s[2:3]
	s_cbranch_execz .LBB0_1494
	v_lshl_add_u64 v[14:15], v[8:9], 0, v[2:3]
	s_waitcnt vmcnt(4)
	v_mov_b32_e32 v13, v248
	v_lshlrev_b32_e32 v14, 16, v13
	v_and_b32_e32 v13, 0xffff0000, v13
	v_mul_f32_e32 v11, v11, v14
	s_waitcnt lgkmcnt(0)
	v_mul_f32_e32 v12, v12, v13
	v_cvt_pk_bf16_f32 v11, v11, v12
	v_lshl_add_u64 v[12:13], v[6:7], 0, v[2:3]
	global_store_dword v[12:13], v11, off
.LBB0_1494:
	s_or_b64 exec, exec, s[0:1]
	v_mul_f32_e32 v11, v60, v5
	s_waitcnt lgkmcnt(0)
	s_nop 1
	v_mov_b32_dpp v12, v11 quad_perm:[1,0,3,2] row_mask:0xf bank_mask:0xf
	s_and_saveexec_b64 s[0:1], s[2:3]
	s_cbranch_execz .LBB0_1496
	v_lshl_add_u64 v[14:15], v[8:9], 0, v[2:3]
	v_mov_b32_e32 v13, v249
	v_lshlrev_b32_e32 v14, 16, v13
	v_and_b32_e32 v13, 0xffff0000, v13
	v_mul_f32_e32 v11, v11, v14
	s_waitcnt lgkmcnt(0)
	v_mul_f32_e32 v12, v12, v13
	v_cvt_pk_bf16_f32 v11, v11, v12
	v_lshl_add_u64 v[12:13], v[6:7], 0, v[2:3]
	global_store_dword v[12:13], v11, off offset:64
.LBB0_1496:
	s_or_b64 exec, exec, s[0:1]
	v_mul_f32_e32 v11, v44, v5
	s_waitcnt lgkmcnt(0)
	s_nop 1
	v_mov_b32_dpp v12, v11 quad_perm:[1,0,3,2] row_mask:0xf bank_mask:0xf
	s_and_saveexec_b64 s[0:1], s[2:3]
	s_cbranch_execz .LBB0_1498
	v_lshl_add_u64 v[14:15], v[8:9], 0, v[2:3]
	v_mov_b32_e32 v13, v250
	v_lshlrev_b32_e32 v14, 16, v13
	v_and_b32_e32 v13, 0xffff0000, v13
	v_mul_f32_e32 v11, v11, v14
	s_waitcnt lgkmcnt(0)
	v_mul_f32_e32 v12, v12, v13
	v_cvt_pk_bf16_f32 v11, v11, v12
	v_lshl_add_u64 v[12:13], v[6:7], 0, v[2:3]
	global_store_dword v[12:13], v11, off offset:128
.LBB0_1498:
	s_or_b64 exec, exec, s[0:1]
	v_mul_f32_e32 v5, v28, v5
	s_nop 1
	v_mov_b32_dpp v11, v5 quad_perm:[1,0,3,2] row_mask:0xf bank_mask:0xf
	s_and_saveexec_b64 s[0:1], s[2:3]
	s_cbranch_execz .LBB0_1500
	v_lshl_add_u64 v[8:9], v[8:9], 0, v[2:3]
	v_lshl_add_u64 v[6:7], v[6:7], 0, v[2:3]
	v_mov_b32_e32 v8, v251
	v_lshlrev_b32_e32 v9, 16, v8
	v_and_b32_e32 v8, 0xffff0000, v8
	v_mul_f32_e32 v5, v5, v9
	s_waitcnt lgkmcnt(0)
	v_mul_f32_e32 v8, v11, v8
	v_cvt_pk_bf16_f32 v5, v5, v8
	global_store_dword v[6:7], v5, off offset:192
.LBB0_1500:
	s_or_b64 exec, exec, s[0:1]
	ds_read_b32 v5, v160 offset:76
	v_add_u32_e32 v6, 19, v4
	v_ashrrev_i32_e32 v7, 31, v6
	v_lshlrev_b64 v[8:9], 11, v[6:7]
	v_lshlrev_b64 v[6:7], 12, v[6:7]
	s_waitcnt lgkmcnt(0)
	v_rcp_f32_e32 v5, v5
	v_lshl_add_u64 v[8:9], s[6:7], 0, v[8:9]
	v_lshl_add_u64 v[6:7], s[8:9], 0, v[6:7]
	v_add_u32_e32 v252, 24, v4
	v_ashrrev_i32_e32 v253, 31, v252
	v_lshlrev_b64 v[252:253], 11, v[252:253]
	v_lshl_add_u64 v[252:253], s[6:7], 0, v[252:253]
	v_lshl_add_u64 v[252:253], v[252:253], 0, v[2:3]
	global_load_dword v248, v[252:253], off
	global_load_dword v249, v[252:253], off offset:64
	global_load_dword v250, v[252:253], off offset:128
	global_load_dword v251, v[252:253], off offset:192
	v_mul_f32_e32 v11, v77, v5
	s_nop 1
	v_mov_b32_dpp v12, v11 quad_perm:[1,0,3,2] row_mask:0xf bank_mask:0xf
	s_and_saveexec_b64 s[0:1], s[2:3]
	s_cbranch_execz .LBB0_1502
	v_lshl_add_u64 v[14:15], v[8:9], 0, v[2:3]
	s_waitcnt vmcnt(4)
	v_mov_b32_e32 v13, v244
	v_lshlrev_b32_e32 v14, 16, v13
	v_and_b32_e32 v13, 0xffff0000, v13
	v_mul_f32_e32 v11, v11, v14
	s_waitcnt lgkmcnt(0)
	v_mul_f32_e32 v12, v12, v13
	v_cvt_pk_bf16_f32 v11, v11, v12
	v_lshl_add_u64 v[12:13], v[6:7], 0, v[2:3]
	global_store_dword v[12:13], v11, off

; __device__ __forceinline__ unsigned cvt_pk_bf16(float lo, float hi) { unsigned r; asm volatile("v_cvt_pk_bf16_f32 %0, %1, %2" : "=v"(r) : "v"(lo), "v"(hi)); return r; }
; __device__ __forceinline__ float bf_lo(unsigned w) { return __uint_as_float(w << 16); }
; __device__ __forceinline__ float bf_hi(unsigned w) { return __uint_as_float(w & 0xffff0000u); }
; __device__ __forceinline__ int crow(int r, int hi) { return (r & 3) + 8 * (r >> 2) + 4 * hi; }
; template <int MODE> ...
;     ...
;     for (int r = 0; r < 16; ++r) { const int orow = qlo + crow(r, hi); const float rl = __builtin_amdgcn_rcpf(li_l[crow(r, hi)]);
; #pragma unroll
;         for (int d0 = 0; d0 < 4; ++d0) { float v = o[d0][r] * rl; float vn = __shfl_xor(v, 1);
;             if ((r32 & 1) == 0) { const int col = d0 * 32 + r32;
;                 if (MODE == 1) { const unsigned g = *(const unsigned*)(gate + (size_t)orow * 1024 + hoff + col); v *= bf_lo(g); vn *= bf_hi(g); }
;                 *(unsigned*)(Ob + (size_t)orow * DM + ocol0 + col) = cvt_pk_bf16(v, vn); } } }
.LBB0_1508:
	s_or_b64 exec, exec, s[0:1]
	ds_read_b32 v5, v160 offset:96
	v_add_u32_e32 v6, 24, v4
	v_ashrrev_i32_e32 v7, 31, v6
	v_lshlrev_b64 v[8:9], 11, v[6:7]
	v_lshlrev_b64 v[6:7], 12, v[6:7]
	s_waitcnt lgkmcnt(0)
	v_rcp_f32_e32 v5, v5
	v_lshl_add_u64 v[8:9], s[6:7], 0, v[8:9]
	v_lshl_add_u64 v[6:7], s[8:9], 0, v[6:7]
	v_add_u32_e32 v252, 25, v4
	v_ashrrev_i32_e32 v253, 31, v252
	v_lshlrev_b64 v[252:253], 11, v[252:253]
	v_lshl_add_u64 v[252:253], s[6:7], 0, v[252:253]
	v_lshl_add_u64 v[252:253], v[252:253], 0, v[2:3]
	global_load_dword v244, v[252:253], off
	global_load_dword v245, v[252:253], off offset:64
	global_load_dword v246, v[252:253], off offset:128
	global_load_dword v247, v[252:253], off offset:192
	v_mul_f32_e32 v11, v78, v5
	s_nop 1
	v_mov_b32_dpp v12, v11 quad_perm:[1,0,3,2] row_mask:0xf bank_mask:0xf
	s_and_saveexec_b64 s[0:1], s[2:3]
	s_cbranch_execz .LBB0_1510
	v_lshl_add_u64 v[14:15], v[8:9], 0, v[2:3]
	s_waitcnt vmcnt(4)
	v_mov_b32_e32 v13, v248
	v_lshlrev_b32_e32 v14, 16, v13
	v_and_b32_e32 v13, 0xffff0000, v13
	v_mul_f32_e32 v11, v11, v14
	s_waitcnt lgkmcnt(0)
	v_mul_f32_e32 v12, v12, v13
	v_cvt_pk_bf16_f32 v11, v11, v12
	v_lshl_add_u64 v[12:13], v[6:7], 0, v[2:3]
	global_store_dword v[12:13], v11, off
.LBB0_1510:
	s_or_b64 exec, exec, s[0:1]
	v_mul_f32_e32 v11, v62, v5
	s_waitcnt lgkmcnt(0)
	s_nop 1
	v_mov_b32_dpp v12, v11 quad_perm:[1,0,3,2] row_mask:0xf bank_mask:0xf
	s_and_saveexec_b64 s[0:1], s[2:3]
	s_cbranch_execz .LBB0_1512
	v_lshl_add_u64 v[14:15], v[8:9], 0, v[2:3]
	v_mov_b32_e32 v13, v249
	v_lshlrev_b32_e32 v14, 16, v13
	v_and_b32_e32 v13, 0xffff0000, v13
	v_mul_f32_e32 v11, v11, v14
	s_waitcnt lgkmcnt(0)
	v_mul_f32_e32 v12, v12, v13
	v_cvt_pk_bf16_f32 v11, v11, v12
	v_lshl_add_u64 v[12:13], v[6:7], 0, v[2:3]
	global_store_dword v[12:13], v11, off offset:64
.LBB0_1512:
	s_or_b64 exec, exec, s[0:1]
	v_mul_f32_e32 v11, v46, v5
	s_waitcnt lgkmcnt(0)
	s_nop 1
	v_mov_b32_dpp v12, v11 quad_perm:[1,0,3,2] row_mask:0xf bank_mask:0xf
	s_and_saveexec_b64 s[0:1], s[2:3]
	s_cbranch_execz .LBB0_1514
	v_lshl_add_u64 v[14:15], v[8:9], 0, v[2:3]
	v_mov_b32_e32 v13, v250
	v_lshlrev_b32_e32 v14, 16, v13
	v_and_b32_e32 v13, 0xffff0000, v13
	v_mul_f32_e32 v11, v11, v14
	s_waitcnt lgkmcnt(0)
	v_mul_f32_e32 v12, v12, v13
	v_cvt_pk_bf16_f32 v11, v11, v12
	v_lshl_add_u64 v[12:13], v[6:7], 0, v[2:3]
	global_store_dword v[12:13], v11, off offset:128
.LBB0_1514:
	s_or_b64 exec, exec, s[0:1]
	v_mul_f32_e32 v5, v30, v5
	s_nop 1
	v_mov_b32_dpp v11, v5 quad_perm:[1,0,3,2] row_mask:0xf bank_mask:0xf
	s_and_saveexec_b64 s[0:1], s[2:3]
	s_cbranch_execz .LBB0_1516
	v_lshl_add_u64 v[8:9], v[8:9], 0, v[2:3]
	v_lshl_add_u64 v[6:7], v[6:7], 0, v[2:3]
	v_mov_b32_e32 v8, v251
	v_lshlrev_b32_e32 v9, 16, v8
	v_and_b32_e32 v8, 0xffff0000, v8
	v_mul_f32_e32 v5, v5, v9
	s_waitcnt lgkmcnt(0)
	v_mul_f32_e32 v8, v11, v8
	v_cvt_pk_bf16_f32 v5, v5, v8
	global_store_dword v[6:7], v5, off offset:192
.LBB0_1516:
	s_or_b64 exec, exec, s[0:1]
	ds_read_b32 v5, v160 offset:100
	v_add_u32_e32 v6, 25, v4
	v_ashrrev_i32_e32 v7, 31, v6
	v_lshlrev_b64 v[8:9], 11, v[6:7]
	v_lshlrev_b64 v[6:7], 12, v[6:7]
	s_waitcnt lgkmcnt(0)
	v_rcp_f32_e32 v5, v5
	v_lshl_add_u64 v[8:9], s[6:7], 0, v[8:9]
	v_lshl_add_u64 v[6:7], s[8:9], 0, v[6:7]
	v_add_u32_e32 v252, 26, v4
	v_ashrrev_i32_e32 v253, 31, v252
	v_lshlrev_b64 v[252:253], 11, v[252:253]
	v_lshl_add_u64 v[252:253], s[6:7], 0, v[252:253]
	v_lshl_add_u64 v[252:253], v[252:253], 0, v[2:3]
	global_load_dword v248, v[252:253], off
	global_load_dword v249, v[252:253], off offset:64
	global_load_dword v250, v[252:253], off offset:128
	global_load_dword v251, v[252:253], off offset:192
	v_mul_f32_e32 v11, v79, v5
	s_nop 1
	v_mov_b32_dpp v12, v11 quad_perm:[1,0,3,2] row_mask:0xf bank_mask:0xf
	s_and_saveexec_b64 s[0:1], s[2:3]
	s_cbranch_execz .LBB0_1518
	v_lshl_add_u64 v[14:15], v[8:9], 0, v[2:3]
	s_waitcnt vmcnt(4)
	v_mov_b32_e32 v13, v244
	v_lshlrev_b32_e32 v14, 16, v13
	v_and_b32_e32 v13, 0xffff0000, v13
	v_mul_f32_e32 v11, v11, v14
	s_waitcnt lgkmcnt(0)
	v_mul_f32_e32 v12, v12, v13
	v_cvt_pk_bf16_f32 v11, v11, v12
	v_lshl_add_u64 v[12:13], v[6:7], 0, v[2:3]
	global_store_dword v[12:13], v11, off

; __device__ __forceinline__ unsigned cvt_pk_bf16(float lo, float hi) { unsigned r; asm volatile("v_cvt_pk_bf16_f32 %0, %1, %2" : "=v"(r) : "v"(lo), "v"(hi)); return r; }
; __device__ __forceinline__ float bf_lo(unsigned w) { return __uint_as_float(w << 16); }
; __device__ __forceinline__ float bf_hi(unsigned w) { return __uint_as_float(w & 0xffff0000u); }
; __device__ __forceinline__ int crow(int r, int hi) { return (r & 3) + 8 * (r >> 2) + 4 * hi; }
; template <int MODE> ...
;     ...
;     for (int r = 0; r < 16; ++r) { const int orow = qlo + crow(r, hi); const float rl = __builtin_amdgcn_rcpf(li_l[crow(r, hi)]);
; #pragma unroll
;         for (int d0 = 0; d0 < 4; ++d0) { float v = o[d0][r] * rl; float vn = __shfl_xor(v, 1);
;             if ((r32 & 1) == 0) { const int col = d0 * 32 + r32;
;                 if (MODE == 1) { const unsigned g = *(const unsigned*)(gate + (size_t)orow * 1024 + hoff + col); v *= bf_lo(g); vn *= bf_hi(g); }
;                 *(unsigned*)(Ob + (size_t)orow * DM + ocol0 + col) = cvt_pk_bf16(v, vn); } } }
.LBB0_1524:
	s_or_b64 exec, exec, s[0:1]
	ds_read_b32 v5, v160 offset:104
	v_add_u32_e32 v6, 26, v4
	v_ashrrev_i32_e32 v7, 31, v6
	v_lshlrev_b64 v[8:9], 11, v[6:7]
	v_lshlrev_b64 v[6:7], 12, v[6:7]
	s_waitcnt lgkmcnt(0)
	v_rcp_f32_e32 v5, v5
	v_lshl_add_u64 v[8:9], s[6:7], 0, v[8:9]
	v_lshl_add_u64 v[6:7], s[8:9], 0, v[6:7]
	v_mul_f32_e32 v11, v80, v5
	s_nop 1
	v_mov_b32_dpp v12, v11 quad_perm:[1,0,3,2] row_mask:0xf bank_mask:0xf
	s_and_saveexec_b64 s[0:1], s[2:3]
	s_cbranch_execz .LBB0_1526
	v_lshl_add_u64 v[14:15], v[8:9], 0, v[2:3]
	s_waitcnt vmcnt(0)
	v_mov_b32_e32 v13, v248
	v_lshlrev_b32_e32 v14, 16, v13
	v_and_b32_e32 v13, 0xffff0000, v13
	v_mul_f32_e32 v11, v11, v14
	s_waitcnt lgkmcnt(0)
	v_mul_f32_e32 v12, v12, v13
	v_cvt_pk_bf16_f32 v11, v11, v12
	v_lshl_add_u64 v[12:13], v[6:7], 0, v[2:3]
	global_store_dword v[12:13], v11, off
.LBB0_1526:
	s_or_b64 exec, exec, s[0:1]
	v_mul_f32_e32 v11, v64, v5
	s_waitcnt lgkmcnt(0)
	s_nop 1
	v_mov_b32_dpp v12, v11 quad_perm:[1,0,3,2] row_mask:0xf bank_mask:0xf
	s_and_saveexec_b64 s[0:1], s[2:3]
	s_cbranch_execz .LBB0_1528
	v_lshl_add_u64 v[14:15], v[8:9], 0, v[2:3]
	v_mov_b32_e32 v13, v249
	v_lshlrev_b32_e32 v14, 16, v13
	v_and_b32_e32 v13, 0xffff0000, v13
	v_mul_f32_e32 v11, v11, v14
	s_waitcnt lgkmcnt(0)
	v_mul_f32_e32 v12, v12, v13
	v_cvt_pk_bf16_f32 v11, v11, v12
	v_lshl_add_u64 v[12:13], v[6:7], 0, v[2:3]
	global_store_dword v[12:13], v11, off offset:64
.LBB0_1528:
	s_or_b64 exec, exec, s[0:1]
	v_mul_f32_e32 v11, v48, v5
	s_waitcnt lgkmcnt(0)
	s_nop 1
	v_mov_b32_dpp v12, v11 quad_perm:[1,0,3,2] row_mask:0xf bank_mask:0xf
	s_and_saveexec_b64 s[0:1], s[2:3]
	s_cbranch_execz .LBB0_1530
	v_lshl_add_u64 v[14:15], v[8:9], 0, v[2:3]
	v_mov_b32_e32 v13, v250
	v_lshlrev_b32_e32 v14, 16, v13
	v_and_b32_e32 v13, 0xffff0000, v13
	v_mul_f32_e32 v11, v11, v14
	s_waitcnt lgkmcnt(0)
	v_mul_f32_e32 v12, v12, v13
	v_cvt_pk_bf16_f32 v11, v11, v12
	v_lshl_add_u64 v[12:13], v[6:7], 0, v[2:3]
	global_store_dword v[12:13], v11, off offset:128
.LBB0_1530:
	s_or_b64 exec, exec, s[0:1]
	v_mul_f32_e32 v5, v32, v5
	s_nop 1
	v_mov_b32_dpp v11, v5 quad_perm:[1,0,3,2] row_mask:0xf bank_mask:0xf
	s_and_saveexec_b64 s[0:1], s[2:3]
	s_cbranch_execz .LBB0_1532
	v_lshl_add_u64 v[8:9], v[8:9], 0, v[2:3]
	v_lshl_add_u64 v[6:7], v[6:7], 0, v[2:3]
	v_mov_b32_e32 v8, v251
	v_lshlrev_b32_e32 v9, 16, v8
	v_and_b32_e32 v8, 0xffff0000, v8
	v_mul_f32_e32 v5, v5, v9
	s_waitcnt lgkmcnt(0)
	v_mul_f32_e32 v8, v11, v8
	v_cvt_pk_bf16_f32 v5, v5, v8
	global_store_dword v[6:7], v5, off offset:192

; #define PG8_STAGE(bufoff, gbase, voff) do { _Pragma("unroll") for (int _i = 0; _i < 2; ++_i) glds16_s((const void*)((const char*)(gbase) + _i * r64), (voff), ldsb + (unsigned)(bufoff) + ldsw + _i * 8192u); } while (0)
; #define PG8_WAIT_V(n) asm volatile("s_waitcnt vmcnt(" #n ")" ::: "memory")
; #define PG8_BAR __builtin_amdgcn_s_barrier()
; template <class Epi, class Sched, bool FP8 = false>
; __device__ __forceinline__ void gemm_phase(LAS unsigned char* lds, const int Kb, const int nt  , const Sched& S, const Epi& E) {
;     ...
;     PG8_STAGE(PG8_SB(0, 0), cB, voffB); PG8_STAGE(PG8_SA(0, 0), cA, voffA); PG8_STAGE(PG8_SB(0, 1), cB + hstep, voffB); PG8_STAGE(PG8_SA(0, 1), cA + hstep, voffA);
;     if (wr == 1) PG8_BAR;
;     PG8_WAIT_V(4); PG8_BAR;
;     PG8_STAGE(PG8_SB(1, 0), cB + kstep, voffB); PG8_STAGE(PG8_SA(1, 0), cA + kstep, voffA); PG8_STAGE(PG8_SB(1, 1), cB + hstep + kstep, voffB);
;     PG8_WAIT_V(6); PG8_BAR;
.LBB0_1706:
	v_readlane_b32 s4, v241, 5
	v_readlane_b32 s5, v241, 6
	s_add_u32 s4, s4, 0x56f00000
	s_addc_u32 s5, s5, 0
	s_lshl_b32 s3, s3, 5
	s_and_b32 s46, s3, 0x60
	s_lshl_b32 s45, s6, 6
	s_lshl_b32 s8, s6, 13
	s_lshl_b32 s3, s46, 7
	s_add_u32 s6, s24, 0x80
	s_addc_u32 s7, s25, 0
	s_add_i32 s47, s37, 0x18000
	s_waitcnt vmcnt(4)
	s_barrier
	s_mov_b32 s9, m0
	s_mov_b32 m0, s47
	s_nop 0
	global_load_lds_dwordx4 v1, s[6:7]
	s_mov_b32 m0, s9
	s_add_u32 s6, s24, 0x40080
	s_addc_u32 s7, s25, 0
	s_add_i32 s48, s37, 0x1a000
	s_mov_b32 s9, m0
	s_mov_b32 m0, s48
	s_nop 0
	global_load_lds_dwordx4 v1, s[6:7]
	s_mov_b32 m0, s9
	s_add_u32 s6, s22, 0x80
	s_addc_u32 s7, s23, 0
	s_add_i32 s49, s37, 0x8000
	s_mov_b32 s9, m0
	s_mov_b32 m0, s49
	s_nop 0
	global_load_lds_dwordx4 v1, s[6:7]
	s_mov_b32 m0, s9
	s_add_u32 s6, s22, 0x40080
	s_addc_u32 s7, s23, 0
	s_add_i32 s50, s37, 0xa000
	s_mov_b32 s9, m0
	s_mov_b32 m0, s50
	s_nop 0
	global_load_lds_dwordx4 v1, s[6:7]
	s_mov_b32 m0, s9
	s_add_u32 s6, s24, 0x80080
	s_addc_u32 s7, s25, 0
	s_add_i32 s51, s37, 0x1c000
	v_lshlrev_b32_e32 v3, 6, v0
	v_lshlrev_b32_e32 v4, 2, v0
	s_mov_b32 s9, m0
	s_mov_b32 m0, s51
	s_nop 0
	global_load_lds_dwordx4 v1, s[6:7]
	s_mov_b32 m0, s9
	s_add_u32 s6, s24, 0xc0080
	v_and_b32_e32 v2, 48, v0
	v_and_b32_e32 v3, 0x3c0, v3
	v_and_b32_e32 v4, 32, v4
	s_addc_u32 s7, s25, 0
	s_add_i32 s52, s37, 0x1e000
	s_mov_b32 s9, m0
	s_mov_b32 m0, s52
	s_nop 0
	global_load_lds_dwordx4 v1, s[6:7]
	s_mov_b32 m0, s9
	v_bitop3_b32 v2, v3, v4, v2 bitop3:0x36
	s_waitcnt vmcnt(6)
	s_add_i32 s3, s3, 0
	s_add_i32 s53, s37, 0xc000
	s_add_i32 s54, s37, 0xe000
	v_add_u32_e32 v3, s3, v2
	v_add_u32_e32 v2, 0, v2
	s_cmp_lg_u64 s[76:77], 0
	s_waitcnt vmcnt(5)
	v_add_u32_e32 v138, 0x10000, v3
	v_add_u32_e32 v139, 0x10400, v3
	v_add_u32_e32 v140, 0x10800, v3
	v_add_u32_e32 v141, 0x10c00, v3
	s_waitcnt vmcnt(4)
	v_add_u32_e32 v142, 0x14000, v3
	v_add_u32_e32 v143, 0x14400, v3
	v_add_u32_e32 v144, 0x14800, v3
	v_add_u32_e32 v145, 0x14c00, v3
	s_waitcnt vmcnt(0)
	v_add_u32_e32 v146, 0x18000, v3
	v_add_u32_e32 v147, 0x18400, v3
	v_add_u32_e32 v148, 0x18800, v3
	v_add_u32_e32 v149, 0x18c00, v3
	v_add_u32_e32 v150, 0x1c000, v3
	v_add_u32_e32 v151, 0x1c400, v3
	v_add_u32_e32 v152, 0x1c800, v3
	v_add_u32_e32 v153, 0x1cc00, v3
	s_cselect_b64 s[6:7], -1, 0
	v_add_u32_e32 v154, s8, v2
	s_mov_b64 s[8:9], 0x48000
	s_mov_b64 s[10:11], 0x50000
	s_mov_b64 s[12:13], 0x58000
	s_mov_b64 s[18:19], s[22:23]
	s_mov_b64 s[20:21], s[24:25]
	s_barrier
	s_branch .LBB0_1708
	s_nop 0
	s_nop 0
	s_nop 0
	s_nop 0
	s_nop 0
	s_nop 0
	s_nop 0
	s_nop 0
